# gate_up bias row staged into LDS by wave 0 with one LDS-DMA ahead of the K-loop, epilogue reads it with ds_read_b128 instead of waiting on global loads
# baseline (speedup 1.0000x reference)
.LBB0_1198:
	s_or_b64 exec, exec, s[2:3]
	s_mov_b32 s85, 0
	s_mov_b64 s[0:1], s[96:97]
	s_mov_b32 s2, s70
	s_mov_b32 s3, -1
	s_waitcnt lgkmcnt(0)
	s_barrier
	s_mov_b32 s20, s73
	v_mbcnt_lo_u32_b32 v0, s3, 0
	v_mbcnt_hi_u32_b32 v0, s3, v0
	v_lshl_add_u32 v2, s2, 6, v0
	s_load_dwordx2 s[12:13], s[0:1], 0xe8
	s_mov_b32 s38, s91
	s_mov_b32 s4, s88
	s_add_i32 s1, s20, 0x20000
	v_cmp_gt_i32_e64 s[2:3], 32, v2
	v_ashrrev_i32_e32 v3, 31, v2
	v_lshl_add_u32 v0, v2, 2, s1
	s_and_saveexec_b64 s[6:7], s[2:3]
	s_cbranch_execz .LBB0_1200
	s_mov_b32 s15, s73
	s_lshl_b64 s[8:9], s[14:15], 2
	s_waitcnt lgkmcnt(0)
	s_add_u32 s8, s12, s8
	s_addc_u32 s9, s13, s9
	v_lshl_add_u64 v[4:5], v[2:3], 2, s[8:9]
	v_add_co_u32_e32 v4, vcc, 0x10000, v4
	s_nop 1
	v_addc_co_u32_e32 v5, vcc, 0, v5, vcc
	global_load_dword v4, v[4:5], off sc1
	s_waitcnt vmcnt(0)
	ds_write_b32 v0, v4 offset:128

.LBB0_1242:
	s_ashr_i32 s23, s22, 31
	s_lshl_b64 s[24:25], s[22:23], 21
	s_add_u32 s23, s1, s24
	s_addc_u32 s30, s33, s25
	s_ashr_i32 s21, s20, 31
	s_lshl_b64 s[24:25], s[20:21], 18
	s_add_u32 s24, s23, s24
	s_addc_u32 s25, s30, s25
	s_and_b64 s[30:31], s[2:3], exec
	s_cselect_b32 s21, s25, s29
	s_cselect_b32 s23, s24, s28
	s_lshl_b32 s64, s63, 10
	s_add_u32 s65, s28, 0x100
	v_mov_b32_e32 v2, 0
	s_addc_u32 s66, s29, 0
	s_mov_b32 s67, -2
	s_mov_b64 s[28:29], s[12:13]
	v_mov_b32_e32 v3, v2
	v_mov_b64_e32 v[4:5], v[2:3]
	v_mov_b64_e32 v[10:11], v[2:3]
	v_mov_b64_e32 v[12:13], v[2:3]
	v_mov_b64_e32 v[18:19], v[2:3]
	v_mov_b64_e32 v[20:21], v[2:3]
	v_mov_b64_e32 v[26:27], v[2:3]
	v_mov_b64_e32 v[28:29], v[2:3]
	v_mov_b64_e32 v[34:35], v[2:3]
	v_mov_b64_e32 v[36:37], v[2:3]
	v_mov_b64_e32 v[42:43], v[2:3]
	v_mov_b64_e32 v[44:45], v[2:3]
	v_mov_b64_e32 v[50:51], v[2:3]
	v_mov_b64_e32 v[52:53], v[2:3]
	v_mov_b64_e32 v[58:59], v[2:3]
	v_mov_b64_e32 v[60:61], v[2:3]
	v_mov_b64_e32 v[6:7], v[2:3]
	v_mov_b64_e32 v[8:9], v[2:3]
	v_mov_b64_e32 v[14:15], v[2:3]
	v_mov_b64_e32 v[16:17], v[2:3]
	v_mov_b64_e32 v[22:23], v[2:3]
	v_mov_b64_e32 v[24:25], v[2:3]
	v_mov_b64_e32 v[30:31], v[2:3]
	v_mov_b64_e32 v[32:33], v[2:3]
	v_mov_b64_e32 v[38:39], v[2:3]
	v_mov_b64_e32 v[40:41], v[2:3]
	v_mov_b64_e32 v[46:47], v[2:3]
	v_mov_b64_e32 v[48:49], v[2:3]
	v_mov_b64_e32 v[54:55], v[2:3]
	v_mov_b64_e32 v[56:57], v[2:3]
	v_mov_b64_e32 v[62:63], v[2:3]
	v_mov_b64_e32 v[64:65], v[2:3]
	v_mov_b64_e32 v[70:71], v[2:3]
	v_mov_b64_e32 v[72:73], v[2:3]
	v_mov_b64_e32 v[86:87], v[2:3]
	v_mov_b64_e32 v[88:89], v[2:3]
	v_mov_b64_e32 v[98:99], v[2:3]
	s_waitcnt vmcnt(0)
	v_mov_b64_e32 v[100:101], v[2:3]
	v_mov_b64_e32 v[106:107], v[2:3]
	v_mov_b64_e32 v[108:109], v[2:3]
	v_mov_b64_e32 v[114:115], v[2:3]
	v_mov_b64_e32 v[116:117], v[2:3]
	v_mov_b64_e32 v[122:123], v[2:3]
	v_mov_b64_e32 v[124:125], v[2:3]
	v_mov_b64_e32 v[130:131], v[2:3]
	v_mov_b64_e32 v[132:133], v[2:3]
	v_mov_b64_e32 v[138:139], v[2:3]
	v_mov_b64_e32 v[140:141], v[2:3]
	v_mov_b64_e32 v[78:79], v[2:3]
	v_mov_b64_e32 v[80:81], v[2:3]
	v_mov_b64_e32 v[94:95], v[2:3]
	v_mov_b64_e32 v[96:97], v[2:3]
	v_mov_b64_e32 v[102:103], v[2:3]
	v_mov_b64_e32 v[104:105], v[2:3]
	v_mov_b64_e32 v[110:111], v[2:3]
	v_mov_b64_e32 v[112:113], v[2:3]
	v_mov_b64_e32 v[118:119], v[2:3]
	v_mov_b64_e32 v[120:121], v[2:3]
	v_mov_b64_e32 v[126:127], v[2:3]
	v_mov_b64_e32 v[128:129], v[2:3]
	v_mov_b64_e32 v[134:135], v[2:3]
	v_mov_b64_e32 v[136:137], v[2:3]
	v_mov_b64_e32 v[142:143], v[2:3]
	v_mov_b64_e32 v[144:145], v[2:3]
	s_xor_b32 s85, s85, 0x400
	s_cmp_eq_u32 s70, 0
	s_cbranch_scc0 .Lgb_skip
	s_load_dwordx2 s[98:99], s[96:97], 0xc0
	v_mbcnt_lo_u32_b32 v248, -1, 0
	v_mbcnt_hi_u32_b32 v248, -1, v248
	v_lshlrev_b32_e32 v248, 4, v248
	v_lshl_add_u32 v249, v66, 13, v248
	s_lshl_b32 s92, s26, 10
	v_add_u32_e32 v249, s92, v249
	s_add_i32 m0, s85, 0x26800
	s_waitcnt lgkmcnt(0)
	s_add_u32 s98, s98, s18
	s_addc_u32 s99, s99, s19
	s_nop 0
	global_load_lds_dwordx4 v249, s[98:99]
.Lgb_skip:
.LBB0_1243:
	v_add_u32_e32 v0, s64, v150
	ds_read2st64_b32 v[68:69], v0 offset0:2 offset1:3
	s_cmp_eq_u32 s67, 4
	s_cselect_b64 s[30:31], -1, 0
	s_and_b64 s[30:31], s[30:31], exec
	s_cselect_b32 s30, s23, s65
	s_waitcnt lgkmcnt(0)
	v_lshl_add_u32 v0, v68, 10, v151
	v_add_u32_e32 v68, s27, v152
	ds_read_b128 v[154:157], v68
	ds_read_b128 v[158:161], v68 offset:1024
	ds_read_b128 v[162:165], v68 offset:2048
	ds_read_b128 v[166:169], v68 offset:3072
	v_add_u32_e32 v68, s43, v152
	s_cselect_b32 s31, s21, s66
	s_add_u32 s68, s28, 0x80
	ds_read_b128 v[170:173], v68
	ds_read_b128 v[174:177], v68 offset:1024
	ds_read_b128 v[186:189], v68 offset:2048
	ds_read_b128 v[190:193], v68 offset:3072
	s_addc_u32 s69, s29, 0
	s_cmp_eq_u32 s67, 4
	s_cselect_b64 s[36:37], -1, 0
	s_and_b64 s[34:35], s[36:37], exec
	s_cselect_b32 s34, s8, s68
	s_cselect_b32 s35, s9, s69
	s_and_b64 s[36:37], s[2:3], s[36:37]
	s_and_b64 s[36:37], s[36:37], exec
	v_lshl_add_u32 v67, v69, 10, v151
	s_cselect_b32 s36, s60, s63
	s_add_i32 m0, s46, 0xc000
	ds_read_b128 v[194:197], v153
	ds_read_b128 v[198:201], v153 offset:1024
	ds_read_b128 v[202:205], v153 offset:2048
	ds_read_b128 v[206:209], v153 offset:3072
	ds_read_b128 v[210:213], v153 offset:4096
	ds_read_b128 v[214:217], v153 offset:5120
	ds_read_b128 v[244:247], v153 offset:6144
	ds_read_b128 v[248:251], v153 offset:7168
	s_nop 0
	global_load_lds_dwordx4 v0, s[28:29]
	s_add_i32 m0, s46, 0xe000
	s_nop 0
	global_load_lds_dwordx4 v67, s[28:29]
	s_waitcnt vmcnt(8)
	s_waitcnt lgkmcnt(0)
	s_barrier
	s_setprio 1
	s_waitcnt lgkmcnt(0)
	v_mfma_f32_16x16x128_f8f6f4 v[142:145], v[154:161], v[194:201], v[142:145]
	v_mfma_f32_16x16x128_f8f6f4 v[134:137], v[162:169], v[194:201], v[134:137]
	v_mfma_f32_16x16x128_f8f6f4 v[126:129], v[154:161], v[202:209], v[126:129]
	v_mfma_f32_16x16x128_f8f6f4 v[118:121], v[162:169], v[202:209], v[118:121]
	v_mfma_f32_16x16x128_f8f6f4 v[110:113], v[154:161], v[210:217], v[110:113]
	v_mfma_f32_16x16x128_f8f6f4 v[102:105], v[162:169], v[210:217], v[102:105]
	v_mfma_f32_16x16x128_f8f6f4 v[178:181], v[154:161], v[244:251], v[94:97]
	v_mfma_f32_16x16x128_f8f6f4 v[182:185], v[162:169], v[244:251], v[78:81]
	s_setprio 0
	s_setprio 1
	v_mfma_f32_16x16x128_f8f6f4 v[138:141], v[170:177], v[194:201], v[138:141]
	v_mfma_f32_16x16x128_f8f6f4 v[130:133], v[186:193], v[194:201], v[130:133]
	v_mfma_f32_16x16x128_f8f6f4 v[122:125], v[170:177], v[202:209], v[122:125]
	v_mfma_f32_16x16x128_f8f6f4 v[114:117], v[186:193], v[202:209], v[114:117]
	v_mfma_f32_16x16x128_f8f6f4 v[106:109], v[170:177], v[210:217], v[106:109]
	v_mfma_f32_16x16x128_f8f6f4 v[194:197], v[186:193], v[210:217], v[98:101]
	v_mfma_f32_16x16x128_f8f6f4 v[198:201], v[170:177], v[244:251], v[86:89]
	v_mfma_f32_16x16x128_f8f6f4 v[202:205], v[186:193], v[244:251], v[70:73]
	s_setprio 0
	s_barrier
	v_lshl_add_u32 v0, s36, 10, v150
	ds_read2st64_b32 v[76:77], v0 offset1:1
	s_nop 2
	ds_read_b128 v[68:71], v153 offset:16384
	ds_read_b128 v[72:75], v153 offset:17408
	v_mov_b32_e32 v101, v148
	s_mov_b32 m0, s41
	s_waitcnt lgkmcnt(0)
	v_lshl_add_u32 v67, v76, 10, v151
	v_lshl_add_u32 v100, v77, 10, v151
	ds_read_b128 v[76:79], v153 offset:18432
	ds_read_b128 v[80:83], v153 offset:19456
	ds_read_b128 v[84:87], v153 offset:20480
	ds_read_b128 v[88:91], v153 offset:21504
	ds_read_b128 v[92:95], v153 offset:22528
	ds_read_b128 v[96:99], v153 offset:23552
	s_add_u32 s36, s30, 0x20000
	global_load_lds_dwordx4 v101, s[30:31]
	v_mov_b32_e32 v101, v149
	s_mov_b32 m0, s42
	s_addc_u32 s37, s31, 0
	global_load_lds_dwordx4 v101, s[30:31]
	v_mov_b32_e32 v101, v148
	s_mov_b32 m0, s44
	s_nop 0
	global_load_lds_dwordx4 v101, s[36:37]
	v_mov_b32_e32 v101, v149
	s_mov_b32 m0, s45
	s_nop 0
	global_load_lds_dwordx4 v101, s[36:37]
	s_mov_b32 m0, s46
	s_nop 0
	global_load_lds_dwordx4 v67, s[34:35]
	s_mov_b32 m0, s47
	s_nop 0
	global_load_lds_dwordx4 v100, s[34:35]
	s_waitcnt vmcnt(8)
	s_waitcnt lgkmcnt(0)
	s_barrier
	s_setprio 1
	v_mfma_f32_16x16x128_f8f6f4 v[62:65], v[154:161], v[68:75], v[62:65]
	v_mfma_f32_16x16x128_f8f6f4 v[54:57], v[162:169], v[68:75], v[54:57]
	s_waitcnt lgkmcnt(0)
	v_mfma_f32_16x16x128_f8f6f4 v[46:49], v[154:161], v[76:83], v[46:49]
	v_mfma_f32_16x16x128_f8f6f4 v[218:221], v[162:169], v[76:83], v[38:41]
	v_mfma_f32_16x16x128_f8f6f4 v[222:225], v[154:161], v[84:91], v[30:33]
	v_mfma_f32_16x16x128_f8f6f4 v[226:229], v[162:169], v[84:91], v[22:25]
	v_mfma_f32_16x16x128_f8f6f4 v[230:233], v[154:161], v[92:99], v[14:17]
	v_mfma_f32_16x16x128_f8f6f4 v[234:237], v[162:169], v[92:99], v[6:9]
	s_setprio 0
	s_setprio 1
	v_mfma_f32_16x16x128_f8f6f4 v[58:61], v[170:177], v[68:75], v[58:61]
	v_mfma_f32_16x16x128_f8f6f4 v[50:53], v[186:193], v[68:75], v[50:53]
	v_mfma_f32_16x16x128_f8f6f4 v[42:45], v[170:177], v[76:83], v[42:45]
	v_mfma_f32_16x16x128_f8f6f4 v[74:77], v[186:193], v[76:83], v[34:37]
	v_mfma_f32_16x16x128_f8f6f4 v[238:241], v[170:177], v[84:91], v[26:29]
	v_mfma_f32_16x16x128_f8f6f4 v[82:85], v[186:193], v[84:91], v[18:21]
	v_mfma_f32_16x16x128_f8f6f4 v[244:247], v[170:177], v[92:99], v[10:13]
	v_mfma_f32_16x16x128_f8f6f4 v[90:93], v[186:193], v[92:99], v[2:5]
	s_setprio 0
	s_barrier
	s_nop 4
	ds_read2st64_b32 v[2:3], v0 offset0:2 offset1:3
	v_add_u32_e32 v10, s52, v152
	s_waitcnt lgkmcnt(0)
	v_lshl_add_u32 v67, v2, 10, v151
	v_lshl_add_u32 v68, v3, 10, v151
	ds_read_b128 v[2:5], v10
	ds_read_b128 v[6:9], v10 offset:1024
	ds_read_b128 v[154:157], v10 offset:2048
	ds_read_b128 v[158:161], v10 offset:3072
	v_add_u32_e32 v10, s57, v152
	ds_read_b128 v[162:165], v10
	ds_read_b128 v[166:169], v10 offset:1024
	ds_read_b128 v[170:173], v10 offset:2048
	ds_read_b128 v[174:177], v10 offset:3072
	s_mov_b32 m0, s48
	ds_read_b128 v[10:13], v153 offset:32768
	ds_read_b128 v[14:17], v153 offset:33792
	ds_read_b128 v[18:21], v153 offset:34816
	ds_read_b128 v[22:25], v153 offset:35840
	ds_read_b128 v[26:29], v153 offset:36864
	ds_read_b128 v[30:33], v153 offset:37888
	ds_read_b128 v[34:37], v153 offset:38912
	ds_read_b128 v[38:41], v153 offset:39936
	s_nop 0
	global_load_lds_dwordx4 v67, s[34:35]
	s_mov_b32 m0, s49
	s_nop 0
	global_load_lds_dwordx4 v68, s[34:35]
	s_waitcnt vmcnt(8)
	s_waitcnt lgkmcnt(0)
	s_barrier
	s_setprio 1
	s_waitcnt lgkmcnt(0)
	v_mfma_f32_16x16x128_f8f6f4 v[142:145], v[2:9], v[10:17], v[142:145]
	v_mfma_f32_16x16x128_f8f6f4 v[134:137], v[154:161], v[10:17], v[134:137]
	v_mfma_f32_16x16x128_f8f6f4 v[126:129], v[2:9], v[18:25], v[126:129]
	v_mfma_f32_16x16x128_f8f6f4 v[118:121], v[154:161], v[18:25], v[118:121]
	v_mfma_f32_16x16x128_f8f6f4 v[110:113], v[2:9], v[26:33], v[110:113]
	v_mfma_f32_16x16x128_f8f6f4 v[102:105], v[154:161], v[26:33], v[102:105]
	v_mfma_f32_16x16x128_f8f6f4 v[94:97], v[2:9], v[34:41], v[178:181]
	v_mfma_f32_16x16x128_f8f6f4 v[78:81], v[154:161], v[34:41], v[182:185]
	s_setprio 0
	s_setprio 1
	v_mfma_f32_16x16x128_f8f6f4 v[138:141], v[162:169], v[10:17], v[138:141]
	v_mfma_f32_16x16x128_f8f6f4 v[130:133], v[170:177], v[10:17], v[130:133]
	v_mfma_f32_16x16x128_f8f6f4 v[122:125], v[162:169], v[18:25], v[122:125]
	v_mfma_f32_16x16x128_f8f6f4 v[114:117], v[170:177], v[18:25], v[114:117]
	v_mfma_f32_16x16x128_f8f6f4 v[106:109], v[162:169], v[26:33], v[106:109]
	v_mfma_f32_16x16x128_f8f6f4 v[98:101], v[170:177], v[26:33], v[194:197]
	v_mfma_f32_16x16x128_f8f6f4 v[86:89], v[162:169], v[34:41], v[198:201]
	v_mfma_f32_16x16x128_f8f6f4 v[70:73], v[170:177], v[34:41], v[202:205]
	s_setprio 0
	s_barrier
	ds_read2st64_b32 v[10:11], v0 offset1:1
	ds_read_b128 v[186:189], v153 offset:49152
	ds_read_b128 v[190:193], v153 offset:50176
	v_mov_b32_e32 v0, v148
	ds_read_b128 v[194:197], v153 offset:51200
	ds_read_b128 v[198:201], v153 offset:52224
	ds_read_b128 v[202:205], v153 offset:53248
	ds_read_b128 v[206:209], v153 offset:54272
	ds_read_b128 v[210:213], v153 offset:55296
	ds_read_b128 v[214:217], v153 offset:56320
	s_mov_b32 m0, s53
	v_lshl_add_u64 v[14:15], s[30:31], 0, v[0:1]
	v_lshl_add_u64 v[14:15], v[14:15], 0, s[82:83]
	v_mov_b32_e32 v0, v149
	global_load_lds_dwordx4 v[14:15], off
	s_mov_b32 m0, s54
	v_lshl_add_u64 v[14:15], s[30:31], 0, v[0:1]
	v_lshl_add_u64 v[14:15], v[14:15], 0, s[82:83]
	s_add_u32 s30, s30, 0x20080
	v_mov_b32_e32 v0, v148
	global_load_lds_dwordx4 v[14:15], off
	s_addc_u32 s31, s31, 0
	s_mov_b32 m0, s58
	s_waitcnt lgkmcnt(0)
	v_lshl_add_u32 v10, v10, 10, v151
	global_load_lds_dwordx4 v0, s[30:31]
	v_mov_b32_e32 v0, v149
	s_mov_b32 m0, s59
	v_lshl_add_u32 v12, v11, 10, v151
	v_mov_b32_e32 v11, v1
	global_load_lds_dwordx4 v0, s[30:31]
	s_mov_b32 m0, s55
	v_lshl_add_u64 v[10:11], s[34:35], 0, v[10:11]
	v_lshl_add_u64 v[10:11], v[10:11], 0, s[82:83]
	v_mov_b32_e32 v13, v1
	global_load_lds_dwordx4 v[10:11], off
	s_mov_b32 m0, s56
	v_lshl_add_u64 v[10:11], s[34:35], 0, v[12:13]
	v_lshl_add_u64 v[10:11], v[10:11], 0, s[82:83]
	global_load_lds_dwordx4 v[10:11], off
	s_waitcnt vmcnt(8)
	s_waitcnt lgkmcnt(0)
	s_barrier
	s_setprio 1
	v_mfma_f32_16x16x128_f8f6f4 v[62:65], v[2:9], v[186:193], v[62:65]
	v_mfma_f32_16x16x128_f8f6f4 v[54:57], v[154:161], v[186:193], v[54:57]
	v_mfma_f32_16x16x128_f8f6f4 v[46:49], v[2:9], v[194:201], v[46:49]
	v_mfma_f32_16x16x128_f8f6f4 v[38:41], v[154:161], v[194:201], v[218:221]
	v_mfma_f32_16x16x128_f8f6f4 v[30:33], v[2:9], v[202:209], v[222:225]
	v_mfma_f32_16x16x128_f8f6f4 v[22:25], v[154:161], v[202:209], v[226:229]
	v_mfma_f32_16x16x128_f8f6f4 v[14:17], v[2:9], v[210:217], v[230:233]
	v_mfma_f32_16x16x128_f8f6f4 v[6:9], v[154:161], v[210:217], v[234:237]
	s_setprio 0
	s_setprio 1
	v_mfma_f32_16x16x128_f8f6f4 v[58:61], v[162:169], v[186:193], v[58:61]
	v_mfma_f32_16x16x128_f8f6f4 v[50:53], v[170:177], v[186:193], v[50:53]
	v_mfma_f32_16x16x128_f8f6f4 v[42:45], v[162:169], v[194:201], v[42:45]
	v_mfma_f32_16x16x128_f8f6f4 v[34:37], v[170:177], v[194:201], v[74:77]
	v_mfma_f32_16x16x128_f8f6f4 v[26:29], v[162:169], v[202:209], v[238:241]
	v_mfma_f32_16x16x128_f8f6f4 v[18:21], v[170:177], v[202:209], v[82:85]
	v_mfma_f32_16x16x128_f8f6f4 v[10:13], v[162:169], v[210:217], v[244:247]
	v_mfma_f32_16x16x128_f8f6f4 v[2:5], v[170:177], v[210:217], v[90:93]
	s_setprio 0
	s_barrier
	s_add_i32 s67, s67, 2
	s_add_u32 s65, s65, 0x100
	s_addc_u32 s66, s66, 0
	s_add_u32 s28, s28, 0x100
	s_addc_u32 s29, s29, 0
	s_cmp_gt_u32 s67, 5
	s_cbranch_scc0 .LBB0_1243
	s_and_b64 vcc, exec, s[16:17]
	s_cbranch_vccz .LBB0_1246
	s_barrier
.LBB0_1246:
	s_mov_b32 s21, -1
	s_mov_b64 s[28:29], s[96:97]
	s_load_dwordx2 s[30:31], s[28:29], 0xc0
	v_mbcnt_lo_u32_b32 v0, s21, 0
	v_mbcnt_hi_u32_b32 v0, s21, v0
	v_lshrrev_b32_e32 v67, 1, v0
	v_and_or_b32 v0, v0, 15, s50
	s_waitcnt lgkmcnt(0)
	s_add_u32 s30, s30, s18
	s_addc_u32 s31, s31, s19
	s_lshl_b32 s21, s26, 7
	v_and_or_b32 v67, v67, 24, s21
	v_or_b32_e32 v146, s51, v67
	v_ashrrev_i32_e32 v67, 31, v66
	v_lshlrev_b64 v[66:67], 13, v[66:67]
	v_lshlrev_b32_e32 v68, 1, v146
	v_lshl_add_u64 v[66:67], s[30:31], 0, v[66:67]
	v_ashrrev_i32_e32 v69, 31, v68
	v_lshl_add_u64 v[66:67], v[68:69], 2, v[66:67]
	v_and_b32_e32 v179, 0xff, v68
	v_lshlrev_b32_e32 v179, 2, v179
	v_add_u32_e32 v179, s85, v179
	v_add_u32_e32 v179, 0x26800, v179
	ds_read_b128 v[90:93], v179
	ds_read_b128 v[82:85], v179 offset:16
	ds_read_b128 v[74:77], v179 offset:32
	ds_read_b128 v[66:69], v179 offset:48
	s_load_dwordx2 s[28:29], s[28:29], 0xe8
	v_ashrrev_i32_e32 v147, 31, v146
	s_andn2_b64 vcc, exec, s[2:3]
	s_mov_b64 s[2:3], -1
	s_mov_b64 s[68:69], s[94:95]
	s_waitcnt lgkmcnt(0)
	v_lshl_add_u64 v[146:147], s[28:29], 0, v[146:147]
	s_mov_b64 s[28:29], 0x72b00000
	v_lshl_add_u64 v[146:147], v[146:147], 0, s[28:29]
	v_mov_b32_e32 v240, v243
	s_waitcnt lgkmcnt(0)
	s_mov_b32 s99, 0
	s_mov_b32 s72, 0xc0c00000
	v_mov_b32_e32 v178, 0x41000000
	v_add_f32_e32 v91, 1.0, v91
	v_add_f32_e32 v93, 1.0, v93
	v_add_f32_e32 v83, 1.0, v83
	v_add_f32_e32 v85, 1.0, v85
	v_add_f32_e32 v75, 1.0, v75
	v_add_f32_e32 v77, 1.0, v77
	v_add_f32_e32 v67, 1.0, v67
	v_add_f32_e32 v69, 1.0, v69
	s_mov_b32 s98, -1
	v_mbcnt_lo_u32_b32 v196, s98, 0
	v_mbcnt_hi_u32_b32 v196, s98, v196
	v_and_b32_e32 v197, 3, v196
	v_lshrrev_b32_e32 v198, 2, v196
	v_lshlrev_b32_e32 v199, 4, v197
	v_or_b32_e32 v199, v199, v198
	v_lshlrev_b32_e32 v199, 2, v199
	v_lshrrev_b32_e32 v196, 4, v196
	v_sub_u32_e32 v196, v197, v196
	v_lshlrev_b32_e32 v196, 3, v196
	v_ashrrev_i32_e32 v197, 31, v196
	v_lshl_add_u64 v[196:197], v[146:147], 0, v[196:197]
	v_or_b32_e32 v176, s50, v198
	v_lshl_add_u32 v176, s62, 8, v176
	v_ashrrev_i32_e32 v177, 31, v176
	v_lshlrev_b64 v[176:177], 10, v[176:177]
	v_lshl_add_u64 v[176:177], v[196:197], 0, v[176:177]
	s_mov_b32 s98, 0x0
	v_lshl_add_u64 v[208:209], v[176:177], 0, s[98:99]
	v_fmamk_f32 v142, v142, 0x3d000000, v90
	v_fmamk_f32 v143, v143, 0x3d000000, v92
	v_fmamk_f32 v144, v144, 0x3d000000, v82
	v_fmamk_f32 v145, v145, 0x3d000000, v84
	v_min_f32_e32 v142, 0x40e00000, v142
	v_min_f32_e32 v143, 0x40e00000, v143
	v_min_f32_e32 v144, 0x40e00000, v144
	v_min_f32_e32 v145, 0x40e00000, v145
	v_mul_f32_e32 v180, 0xc01d265f, v142
	v_mul_f32_e32 v181, 0xc01d265f, v143
	v_mul_f32_e32 v182, 0xc01d265f, v144
	v_mul_f32_e32 v183, 0xc01d265f, v145
	v_exp_f32_e32 v180, v180
	v_exp_f32_e32 v181, v181
	v_exp_f32_e32 v182, v182
	v_exp_f32_e32 v183, v183
	v_fmamk_f32 v138, v138, 0x3d000000, v91
	v_fmamk_f32 v139, v139, 0x3d000000, v93
	v_fmamk_f32 v140, v140, 0x3d000000, v83
	v_fmamk_f32 v141, v141, 0x3d000000, v85
	v_add_f32_e32 v180, 1.0, v180
	v_add_f32_e32 v181, 1.0, v181
	v_add_f32_e32 v182, 1.0, v182
	v_add_f32_e32 v183, 1.0, v183
	v_rcp_f32_e32 v180, v180
	v_rcp_f32_e32 v181, v181
	v_rcp_f32_e32 v182, v182
	v_rcp_f32_e32 v183, v183
	v_med3_f32 v138, v138, s72, v178
	v_med3_f32 v139, v139, s72, v178
	v_med3_f32 v140, v140, s72, v178
	v_med3_f32 v141, v141, s72, v178
	v_mul_f32_e32 v180, v142, v180
	v_mul_f32_e32 v181, v143, v181
	v_mul_f32_e32 v182, v144, v182
	v_mul_f32_e32 v183, v145, v183
	v_mul_f32_e32 v180, v138, v180
	v_mul_f32_e32 v181, v139, v181
	v_mul_f32_e32 v182, v140, v182
	v_mul_f32_e32 v183, v141, v183
	v_cvt_pk_fp8_f32 v200, v180, v181
	v_cvt_pk_fp8_f32 v200, v182, v183 op_sel:[0,0,1]
	v_fmamk_f32 v134, v134, 0x3d000000, v74
	v_fmamk_f32 v135, v135, 0x3d000000, v76
	v_fmamk_f32 v136, v136, 0x3d000000, v66
	v_fmamk_f32 v137, v137, 0x3d000000, v68
	v_min_f32_e32 v134, 0x40e00000, v134
	v_min_f32_e32 v135, 0x40e00000, v135
	v_min_f32_e32 v136, 0x40e00000, v136
	v_min_f32_e32 v137, 0x40e00000, v137
	v_mul_f32_e32 v184, 0xc01d265f, v134
	v_mul_f32_e32 v185, 0xc01d265f, v135
	v_mul_f32_e32 v186, 0xc01d265f, v136
	v_mul_f32_e32 v187, 0xc01d265f, v137
	v_exp_f32_e32 v184, v184
	v_exp_f32_e32 v185, v185
	v_exp_f32_e32 v186, v186
	v_exp_f32_e32 v187, v187
	v_fmamk_f32 v130, v130, 0x3d000000, v75
	v_fmamk_f32 v131, v131, 0x3d000000, v77
	v_fmamk_f32 v132, v132, 0x3d000000, v67
	v_fmamk_f32 v133, v133, 0x3d000000, v69
	v_add_f32_e32 v184, 1.0, v184
	v_add_f32_e32 v185, 1.0, v185
	v_add_f32_e32 v186, 1.0, v186
	v_add_f32_e32 v187, 1.0, v187
	v_rcp_f32_e32 v184, v184
	v_rcp_f32_e32 v185, v185
	v_rcp_f32_e32 v186, v186
	v_rcp_f32_e32 v187, v187
	v_med3_f32 v130, v130, s72, v178
	v_med3_f32 v131, v131, s72, v178
	v_med3_f32 v132, v132, s72, v178
	v_med3_f32 v133, v133, s72, v178
	v_mul_f32_e32 v184, v134, v184
	v_mul_f32_e32 v185, v135, v185
	v_mul_f32_e32 v186, v136, v186
	v_mul_f32_e32 v187, v137, v187
	v_mul_f32_e32 v184, v130, v184
	v_mul_f32_e32 v185, v131, v185
	v_mul_f32_e32 v186, v132, v186
	v_mul_f32_e32 v187, v133, v187
	v_cvt_pk_fp8_f32 v201, v184, v185
	v_cvt_pk_fp8_f32 v201, v186, v187 op_sel:[0,0,1]
	ds_bpermute_b32 v200, v199, v200
	ds_bpermute_b32 v201, v199, v201
	s_mov_b32 s98, 0x4000
	v_lshl_add_u64 v[210:211], v[176:177], 0, s[98:99]
	v_fmamk_f32 v126, v126, 0x3d000000, v90
	v_fmamk_f32 v127, v127, 0x3d000000, v92
	v_fmamk_f32 v128, v128, 0x3d000000, v82
	v_fmamk_f32 v129, v129, 0x3d000000, v84
	v_min_f32_e32 v126, 0x40e00000, v126
	v_min_f32_e32 v127, 0x40e00000, v127
	v_min_f32_e32 v128, 0x40e00000, v128
	v_min_f32_e32 v129, 0x40e00000, v129
	v_mul_f32_e32 v180, 0xc01d265f, v126
	v_mul_f32_e32 v181, 0xc01d265f, v127
	v_mul_f32_e32 v182, 0xc01d265f, v128
	v_mul_f32_e32 v183, 0xc01d265f, v129
	v_exp_f32_e32 v180, v180
	v_exp_f32_e32 v181, v181
	v_exp_f32_e32 v182, v182
	v_exp_f32_e32 v183, v183
	v_fmamk_f32 v122, v122, 0x3d000000, v91
	v_fmamk_f32 v123, v123, 0x3d000000, v93
	v_fmamk_f32 v124, v124, 0x3d000000, v83
	v_fmamk_f32 v125, v125, 0x3d000000, v85
	v_add_f32_e32 v180, 1.0, v180
	v_add_f32_e32 v181, 1.0, v181
	v_add_f32_e32 v182, 1.0, v182
	v_add_f32_e32 v183, 1.0, v183
	v_rcp_f32_e32 v180, v180
	v_rcp_f32_e32 v181, v181
	v_rcp_f32_e32 v182, v182
	v_rcp_f32_e32 v183, v183
	v_med3_f32 v122, v122, s72, v178
	v_med3_f32 v123, v123, s72, v178
	v_med3_f32 v124, v124, s72, v178
	v_med3_f32 v125, v125, s72, v178
	v_mul_f32_e32 v180, v126, v180
	v_mul_f32_e32 v181, v127, v181
	v_mul_f32_e32 v182, v128, v182
	v_mul_f32_e32 v183, v129, v183
	v_mul_f32_e32 v180, v122, v180
	v_mul_f32_e32 v181, v123, v181
	v_mul_f32_e32 v182, v124, v182
	v_mul_f32_e32 v183, v125, v183
	v_cvt_pk_fp8_f32 v202, v180, v181
	v_cvt_pk_fp8_f32 v202, v182, v183 op_sel:[0,0,1]
	v_fmamk_f32 v118, v118, 0x3d000000, v74
	v_fmamk_f32 v119, v119, 0x3d000000, v76
	v_fmamk_f32 v120, v120, 0x3d000000, v66
	v_fmamk_f32 v121, v121, 0x3d000000, v68
	v_min_f32_e32 v118, 0x40e00000, v118
	v_min_f32_e32 v119, 0x40e00000, v119
	v_min_f32_e32 v120, 0x40e00000, v120
	v_min_f32_e32 v121, 0x40e00000, v121
	v_mul_f32_e32 v184, 0xc01d265f, v118
	v_mul_f32_e32 v185, 0xc01d265f, v119
	v_mul_f32_e32 v186, 0xc01d265f, v120
	v_mul_f32_e32 v187, 0xc01d265f, v121
	v_exp_f32_e32 v184, v184
	v_exp_f32_e32 v185, v185
	v_exp_f32_e32 v186, v186
	v_exp_f32_e32 v187, v187
	v_fmamk_f32 v114, v114, 0x3d000000, v75
	v_fmamk_f32 v115, v115, 0x3d000000, v77
	v_fmamk_f32 v116, v116, 0x3d000000, v67
	v_fmamk_f32 v117, v117, 0x3d000000, v69
	v_add_f32_e32 v184, 1.0, v184
	v_add_f32_e32 v185, 1.0, v185
	v_add_f32_e32 v186, 1.0, v186
	v_add_f32_e32 v187, 1.0, v187
	v_rcp_f32_e32 v184, v184
	v_rcp_f32_e32 v185, v185
	v_rcp_f32_e32 v186, v186
	v_rcp_f32_e32 v187, v187
	v_med3_f32 v114, v114, s72, v178
	v_med3_f32 v115, v115, s72, v178
	v_med3_f32 v116, v116, s72, v178
	v_med3_f32 v117, v117, s72, v178
	v_mul_f32_e32 v184, v118, v184
	v_mul_f32_e32 v185, v119, v185
	v_mul_f32_e32 v186, v120, v186
	v_mul_f32_e32 v187, v121, v187
	v_mul_f32_e32 v184, v114, v184
	v_mul_f32_e32 v185, v115, v185
	v_mul_f32_e32 v186, v116, v186
	v_mul_f32_e32 v187, v117, v187
	v_cvt_pk_fp8_f32 v203, v184, v185
	v_cvt_pk_fp8_f32 v203, v186, v187 op_sel:[0,0,1]
	ds_bpermute_b32 v202, v199, v202
	ds_bpermute_b32 v203, v199, v203
	s_waitcnt lgkmcnt(2)
	global_store_dwordx2 v[208:209], v[200:201], off
	s_mov_b32 s98, 0x8000
	v_lshl_add_u64 v[212:213], v[176:177], 0, s[98:99]
	v_fmamk_f32 v110, v110, 0x3d000000, v90
	v_fmamk_f32 v111, v111, 0x3d000000, v92
	v_fmamk_f32 v112, v112, 0x3d000000, v82
	v_fmamk_f32 v113, v113, 0x3d000000, v84
	v_min_f32_e32 v110, 0x40e00000, v110
	v_min_f32_e32 v111, 0x40e00000, v111
	v_min_f32_e32 v112, 0x40e00000, v112
	v_min_f32_e32 v113, 0x40e00000, v113
	v_mul_f32_e32 v180, 0xc01d265f, v110
	v_mul_f32_e32 v181, 0xc01d265f, v111
	v_mul_f32_e32 v182, 0xc01d265f, v112
	v_mul_f32_e32 v183, 0xc01d265f, v113
	v_exp_f32_e32 v180, v180
	v_exp_f32_e32 v181, v181
	v_exp_f32_e32 v182, v182
	v_exp_f32_e32 v183, v183
	v_fmamk_f32 v106, v106, 0x3d000000, v91
	v_fmamk_f32 v107, v107, 0x3d000000, v93
	v_fmamk_f32 v108, v108, 0x3d000000, v83
	v_fmamk_f32 v109, v109, 0x3d000000, v85
	v_add_f32_e32 v180, 1.0, v180
	v_add_f32_e32 v181, 1.0, v181
	v_add_f32_e32 v182, 1.0, v182
	v_add_f32_e32 v183, 1.0, v183
	v_rcp_f32_e32 v180, v180
	v_rcp_f32_e32 v181, v181
	v_rcp_f32_e32 v182, v182
	v_rcp_f32_e32 v183, v183
	v_med3_f32 v106, v106, s72, v178
	v_med3_f32 v107, v107, s72, v178
	v_med3_f32 v108, v108, s72, v178
	v_med3_f32 v109, v109, s72, v178
	v_mul_f32_e32 v180, v110, v180
	v_mul_f32_e32 v181, v111, v181
	v_mul_f32_e32 v182, v112, v182
	v_mul_f32_e32 v183, v113, v183
	v_mul_f32_e32 v180, v106, v180
	v_mul_f32_e32 v181, v107, v181
	v_mul_f32_e32 v182, v108, v182
	v_mul_f32_e32 v183, v109, v183
	v_cvt_pk_fp8_f32 v204, v180, v181
	v_cvt_pk_fp8_f32 v204, v182, v183 op_sel:[0,0,1]
	v_fmamk_f32 v102, v102, 0x3d000000, v74
	v_fmamk_f32 v103, v103, 0x3d000000, v76
	v_fmamk_f32 v104, v104, 0x3d000000, v66
	v_fmamk_f32 v105, v105, 0x3d000000, v68
	v_min_f32_e32 v102, 0x40e00000, v102
	v_min_f32_e32 v103, 0x40e00000, v103
	v_min_f32_e32 v104, 0x40e00000, v104
	v_min_f32_e32 v105, 0x40e00000, v105
	v_mul_f32_e32 v184, 0xc01d265f, v102
	v_mul_f32_e32 v185, 0xc01d265f, v103
	v_mul_f32_e32 v186, 0xc01d265f, v104
	v_mul_f32_e32 v187, 0xc01d265f, v105
	v_exp_f32_e32 v184, v184
	v_exp_f32_e32 v185, v185
	v_exp_f32_e32 v186, v186
	v_exp_f32_e32 v187, v187
	v_fmamk_f32 v98, v98, 0x3d000000, v75
	v_fmamk_f32 v99, v99, 0x3d000000, v77
	v_fmamk_f32 v100, v100, 0x3d000000, v67
	v_fmamk_f32 v101, v101, 0x3d000000, v69
	v_add_f32_e32 v184, 1.0, v184
	v_add_f32_e32 v185, 1.0, v185
	v_add_f32_e32 v186, 1.0, v186
	v_add_f32_e32 v187, 1.0, v187
	v_rcp_f32_e32 v184, v184
	v_rcp_f32_e32 v185, v185
	v_rcp_f32_e32 v186, v186
	v_rcp_f32_e32 v187, v187
	v_med3_f32 v98, v98, s72, v178
	v_med3_f32 v99, v99, s72, v178
	v_med3_f32 v100, v100, s72, v178
	v_med3_f32 v101, v101, s72, v178
	v_mul_f32_e32 v184, v102, v184
	v_mul_f32_e32 v185, v103, v185
	v_mul_f32_e32 v186, v104, v186
	v_mul_f32_e32 v187, v105, v187
	v_mul_f32_e32 v184, v98, v184
	v_mul_f32_e32 v185, v99, v185
	v_mul_f32_e32 v186, v100, v186
	v_mul_f32_e32 v187, v101, v187
	v_cvt_pk_fp8_f32 v205, v184, v185
	v_cvt_pk_fp8_f32 v205, v186, v187 op_sel:[0,0,1]
	ds_bpermute_b32 v204, v199, v204
	ds_bpermute_b32 v205, v199, v205
	s_waitcnt lgkmcnt(2)
	global_store_dwordx2 v[210:211], v[202:203], off
	s_mov_b32 s98, 0xc000
	v_lshl_add_u64 v[214:215], v[176:177], 0, s[98:99]
	v_fmamk_f32 v94, v94, 0x3d000000, v90
	v_fmamk_f32 v95, v95, 0x3d000000, v92
	v_fmamk_f32 v96, v96, 0x3d000000, v82
	v_fmamk_f32 v97, v97, 0x3d000000, v84
	v_min_f32_e32 v94, 0x40e00000, v94
	v_min_f32_e32 v95, 0x40e00000, v95
	v_min_f32_e32 v96, 0x40e00000, v96
	v_min_f32_e32 v97, 0x40e00000, v97
	v_mul_f32_e32 v180, 0xc01d265f, v94
	v_mul_f32_e32 v181, 0xc01d265f, v95
	v_mul_f32_e32 v182, 0xc01d265f, v96
	v_mul_f32_e32 v183, 0xc01d265f, v97
	v_exp_f32_e32 v180, v180
	v_exp_f32_e32 v181, v181
	v_exp_f32_e32 v182, v182
	v_exp_f32_e32 v183, v183
	v_fmamk_f32 v86, v86, 0x3d000000, v91
	v_fmamk_f32 v87, v87, 0x3d000000, v93
	v_fmamk_f32 v88, v88, 0x3d000000, v83
	v_fmamk_f32 v89, v89, 0x3d000000, v85
	v_add_f32_e32 v180, 1.0, v180
	v_add_f32_e32 v181, 1.0, v181
	v_add_f32_e32 v182, 1.0, v182
	v_add_f32_e32 v183, 1.0, v183
	v_rcp_f32_e32 v180, v180
	v_rcp_f32_e32 v181, v181
	v_rcp_f32_e32 v182, v182
	v_rcp_f32_e32 v183, v183
	v_med3_f32 v86, v86, s72, v178
	v_med3_f32 v87, v87, s72, v178
	v_med3_f32 v88, v88, s72, v178
	v_med3_f32 v89, v89, s72, v178
	v_mul_f32_e32 v180, v94, v180
	v_mul_f32_e32 v181, v95, v181
	v_mul_f32_e32 v182, v96, v182
	v_mul_f32_e32 v183, v97, v183
	v_mul_f32_e32 v180, v86, v180
	v_mul_f32_e32 v181, v87, v181
	v_mul_f32_e32 v182, v88, v182
	v_mul_f32_e32 v183, v89, v183
	v_cvt_pk_fp8_f32 v200, v180, v181
	v_cvt_pk_fp8_f32 v200, v182, v183 op_sel:[0,0,1]
	v_fmamk_f32 v78, v78, 0x3d000000, v74
	v_fmamk_f32 v79, v79, 0x3d000000, v76
	v_fmamk_f32 v80, v80, 0x3d000000, v66
	v_fmamk_f32 v81, v81, 0x3d000000, v68
	v_min_f32_e32 v78, 0x40e00000, v78
	v_min_f32_e32 v79, 0x40e00000, v79
	v_min_f32_e32 v80, 0x40e00000, v80
	v_min_f32_e32 v81, 0x40e00000, v81
	v_mul_f32_e32 v184, 0xc01d265f, v78
	v_mul_f32_e32 v185, 0xc01d265f, v79
	v_mul_f32_e32 v186, 0xc01d265f, v80
	v_mul_f32_e32 v187, 0xc01d265f, v81
	v_exp_f32_e32 v184, v184
	v_exp_f32_e32 v185, v185
	v_exp_f32_e32 v186, v186
	v_exp_f32_e32 v187, v187
	v_fmamk_f32 v70, v70, 0x3d000000, v75
	v_fmamk_f32 v71, v71, 0x3d000000, v77
	v_fmamk_f32 v72, v72, 0x3d000000, v67
	v_fmamk_f32 v73, v73, 0x3d000000, v69
	v_add_f32_e32 v184, 1.0, v184
	v_add_f32_e32 v185, 1.0, v185
	v_add_f32_e32 v186, 1.0, v186
	v_add_f32_e32 v187, 1.0, v187
	v_rcp_f32_e32 v184, v184
	v_rcp_f32_e32 v185, v185
	v_rcp_f32_e32 v186, v186
	v_rcp_f32_e32 v187, v187
	v_med3_f32 v70, v70, s72, v178
	v_med3_f32 v71, v71, s72, v178
	v_med3_f32 v72, v72, s72, v178
	v_med3_f32 v73, v73, s72, v178
	v_mul_f32_e32 v184, v78, v184
	v_mul_f32_e32 v185, v79, v185
	v_mul_f32_e32 v186, v80, v186
	v_mul_f32_e32 v187, v81, v187
	v_mul_f32_e32 v184, v70, v184
	v_mul_f32_e32 v185, v71, v185
	v_mul_f32_e32 v186, v72, v186
	v_mul_f32_e32 v187, v73, v187
	v_cvt_pk_fp8_f32 v201, v184, v185
	v_cvt_pk_fp8_f32 v201, v186, v187 op_sel:[0,0,1]
	ds_bpermute_b32 v200, v199, v200
	ds_bpermute_b32 v201, v199, v201
	s_waitcnt lgkmcnt(2)
	global_store_dwordx2 v[212:213], v[204:205], off
	s_mov_b32 s98, 0x20000
	v_lshl_add_u64 v[208:209], v[176:177], 0, s[98:99]
	v_fmamk_f32 v62, v62, 0x3d000000, v90
	v_fmamk_f32 v63, v63, 0x3d000000, v92
	v_fmamk_f32 v64, v64, 0x3d000000, v82
	v_fmamk_f32 v65, v65, 0x3d000000, v84
	v_min_f32_e32 v62, 0x40e00000, v62
	v_min_f32_e32 v63, 0x40e00000, v63
	v_min_f32_e32 v64, 0x40e00000, v64
	v_min_f32_e32 v65, 0x40e00000, v65
	v_mul_f32_e32 v180, 0xc01d265f, v62
	v_mul_f32_e32 v181, 0xc01d265f, v63
	v_mul_f32_e32 v182, 0xc01d265f, v64
	v_mul_f32_e32 v183, 0xc01d265f, v65
	v_exp_f32_e32 v180, v180
	v_exp_f32_e32 v181, v181
	v_exp_f32_e32 v182, v182
	v_exp_f32_e32 v183, v183
	v_fmamk_f32 v58, v58, 0x3d000000, v91
	v_fmamk_f32 v59, v59, 0x3d000000, v93
	v_fmamk_f32 v60, v60, 0x3d000000, v83
	v_fmamk_f32 v61, v61, 0x3d000000, v85
	v_add_f32_e32 v180, 1.0, v180
	v_add_f32_e32 v181, 1.0, v181
	v_add_f32_e32 v182, 1.0, v182
	v_add_f32_e32 v183, 1.0, v183
	v_rcp_f32_e32 v180, v180
	v_rcp_f32_e32 v181, v181
	v_rcp_f32_e32 v182, v182
	v_rcp_f32_e32 v183, v183
	v_med3_f32 v58, v58, s72, v178
	v_med3_f32 v59, v59, s72, v178
	v_med3_f32 v60, v60, s72, v178
	v_med3_f32 v61, v61, s72, v178
	v_mul_f32_e32 v180, v62, v180
	v_mul_f32_e32 v181, v63, v181
	v_mul_f32_e32 v182, v64, v182
	v_mul_f32_e32 v183, v65, v183
	v_mul_f32_e32 v180, v58, v180
	v_mul_f32_e32 v181, v59, v181
	v_mul_f32_e32 v182, v60, v182
	v_mul_f32_e32 v183, v61, v183
	v_cvt_pk_fp8_f32 v202, v180, v181
	v_cvt_pk_fp8_f32 v202, v182, v183 op_sel:[0,0,1]
	v_fmamk_f32 v54, v54, 0x3d000000, v74
	v_fmamk_f32 v55, v55, 0x3d000000, v76
	v_fmamk_f32 v56, v56, 0x3d000000, v66
	v_fmamk_f32 v57, v57, 0x3d000000, v68
	v_min_f32_e32 v54, 0x40e00000, v54
	v_min_f32_e32 v55, 0x40e00000, v55
	v_min_f32_e32 v56, 0x40e00000, v56
	v_min_f32_e32 v57, 0x40e00000, v57
	v_mul_f32_e32 v184, 0xc01d265f, v54
	v_mul_f32_e32 v185, 0xc01d265f, v55
	v_mul_f32_e32 v186, 0xc01d265f, v56
	v_mul_f32_e32 v187, 0xc01d265f, v57
	v_exp_f32_e32 v184, v184
	v_exp_f32_e32 v185, v185
	v_exp_f32_e32 v186, v186
	v_exp_f32_e32 v187, v187
	v_fmamk_f32 v50, v50, 0x3d000000, v75
	v_fmamk_f32 v51, v51, 0x3d000000, v77
	v_fmamk_f32 v52, v52, 0x3d000000, v67
	v_fmamk_f32 v53, v53, 0x3d000000, v69
	v_add_f32_e32 v184, 1.0, v184
	v_add_f32_e32 v185, 1.0, v185
	v_add_f32_e32 v186, 1.0, v186
	v_add_f32_e32 v187, 1.0, v187
	v_rcp_f32_e32 v184, v184
	v_rcp_f32_e32 v185, v185
	v_rcp_f32_e32 v186, v186
	v_rcp_f32_e32 v187, v187
	v_med3_f32 v50, v50, s72, v178
	v_med3_f32 v51, v51, s72, v178
	v_med3_f32 v52, v52, s72, v178
	v_med3_f32 v53, v53, s72, v178
	v_mul_f32_e32 v184, v54, v184
	v_mul_f32_e32 v185, v55, v185
	v_mul_f32_e32 v186, v56, v186
	v_mul_f32_e32 v187, v57, v187
	v_mul_f32_e32 v184, v50, v184
	v_mul_f32_e32 v185, v51, v185
	v_mul_f32_e32 v186, v52, v186
	v_mul_f32_e32 v187, v53, v187
	v_cvt_pk_fp8_f32 v203, v184, v185
	v_cvt_pk_fp8_f32 v203, v186, v187 op_sel:[0,0,1]
	ds_bpermute_b32 v202, v199, v202
	ds_bpermute_b32 v203, v199, v203
	s_waitcnt lgkmcnt(2)
	global_store_dwordx2 v[214:215], v[200:201], off
	s_mov_b32 s98, 0x24000
	v_lshl_add_u64 v[210:211], v[176:177], 0, s[98:99]
	v_fmamk_f32 v46, v46, 0x3d000000, v90
	v_fmamk_f32 v47, v47, 0x3d000000, v92
	v_fmamk_f32 v48, v48, 0x3d000000, v82
	v_fmamk_f32 v49, v49, 0x3d000000, v84
	v_min_f32_e32 v46, 0x40e00000, v46
	v_min_f32_e32 v47, 0x40e00000, v47
	v_min_f32_e32 v48, 0x40e00000, v48
	v_min_f32_e32 v49, 0x40e00000, v49
	v_mul_f32_e32 v180, 0xc01d265f, v46
	v_mul_f32_e32 v181, 0xc01d265f, v47
	v_mul_f32_e32 v182, 0xc01d265f, v48
	v_mul_f32_e32 v183, 0xc01d265f, v49
	v_exp_f32_e32 v180, v180
	v_exp_f32_e32 v181, v181
	v_exp_f32_e32 v182, v182
	v_exp_f32_e32 v183, v183
	v_fmamk_f32 v42, v42, 0x3d000000, v91
	v_fmamk_f32 v43, v43, 0x3d000000, v93
	v_fmamk_f32 v44, v44, 0x3d000000, v83
	v_fmamk_f32 v45, v45, 0x3d000000, v85
	v_add_f32_e32 v180, 1.0, v180
	v_add_f32_e32 v181, 1.0, v181
	v_add_f32_e32 v182, 1.0, v182
	v_add_f32_e32 v183, 1.0, v183
	v_rcp_f32_e32 v180, v180
	v_rcp_f32_e32 v181, v181
	v_rcp_f32_e32 v182, v182
	v_rcp_f32_e32 v183, v183
	v_med3_f32 v42, v42, s72, v178
	v_med3_f32 v43, v43, s72, v178
	v_med3_f32 v44, v44, s72, v178
	v_med3_f32 v45, v45, s72, v178
	v_mul_f32_e32 v180, v46, v180
	v_mul_f32_e32 v181, v47, v181
	v_mul_f32_e32 v182, v48, v182
	v_mul_f32_e32 v183, v49, v183
	v_mul_f32_e32 v180, v42, v180
	v_mul_f32_e32 v181, v43, v181
	v_mul_f32_e32 v182, v44, v182
	v_mul_f32_e32 v183, v45, v183
	v_cvt_pk_fp8_f32 v204, v180, v181
	v_cvt_pk_fp8_f32 v204, v182, v183 op_sel:[0,0,1]
	v_fmamk_f32 v38, v38, 0x3d000000, v74
	v_fmamk_f32 v39, v39, 0x3d000000, v76
	v_fmamk_f32 v40, v40, 0x3d000000, v66
	v_fmamk_f32 v41, v41, 0x3d000000, v68
	v_min_f32_e32 v38, 0x40e00000, v38
	v_min_f32_e32 v39, 0x40e00000, v39
	v_min_f32_e32 v40, 0x40e00000, v40
	v_min_f32_e32 v41, 0x40e00000, v41
	v_mul_f32_e32 v184, 0xc01d265f, v38
	v_mul_f32_e32 v185, 0xc01d265f, v39
	v_mul_f32_e32 v186, 0xc01d265f, v40
	v_mul_f32_e32 v187, 0xc01d265f, v41
	v_exp_f32_e32 v184, v184
	v_exp_f32_e32 v185, v185
	v_exp_f32_e32 v186, v186
	v_exp_f32_e32 v187, v187
	v_fmamk_f32 v34, v34, 0x3d000000, v75
	v_fmamk_f32 v35, v35, 0x3d000000, v77
	v_fmamk_f32 v36, v36, 0x3d000000, v67
	v_fmamk_f32 v37, v37, 0x3d000000, v69
	v_add_f32_e32 v184, 1.0, v184
	v_add_f32_e32 v185, 1.0, v185
	v_add_f32_e32 v186, 1.0, v186
	v_add_f32_e32 v187, 1.0, v187
	v_rcp_f32_e32 v184, v184
	v_rcp_f32_e32 v185, v185
	v_rcp_f32_e32 v186, v186
	v_rcp_f32_e32 v187, v187
	v_med3_f32 v34, v34, s72, v178
	v_med3_f32 v35, v35, s72, v178
	v_med3_f32 v36, v36, s72, v178
	v_med3_f32 v37, v37, s72, v178
	v_mul_f32_e32 v184, v38, v184
	v_mul_f32_e32 v185, v39, v185
	v_mul_f32_e32 v186, v40, v186
	v_mul_f32_e32 v187, v41, v187
	v_mul_f32_e32 v184, v34, v184
	v_mul_f32_e32 v185, v35, v185
	v_mul_f32_e32 v186, v36, v186
	v_mul_f32_e32 v187, v37, v187
	v_cvt_pk_fp8_f32 v205, v184, v185
	v_cvt_pk_fp8_f32 v205, v186, v187 op_sel:[0,0,1]
	ds_bpermute_b32 v204, v199, v204
	ds_bpermute_b32 v205, v199, v205
	s_waitcnt lgkmcnt(2)
	global_store_dwordx2 v[208:209], v[202:203], off
	s_mov_b32 s98, 0x28000
	v_lshl_add_u64 v[212:213], v[176:177], 0, s[98:99]
	v_fmamk_f32 v30, v30, 0x3d000000, v90
	v_fmamk_f32 v31, v31, 0x3d000000, v92
	v_fmamk_f32 v32, v32, 0x3d000000, v82
	v_fmamk_f32 v33, v33, 0x3d000000, v84
	v_min_f32_e32 v30, 0x40e00000, v30
	v_min_f32_e32 v31, 0x40e00000, v31
	v_min_f32_e32 v32, 0x40e00000, v32
	v_min_f32_e32 v33, 0x40e00000, v33
	v_mul_f32_e32 v180, 0xc01d265f, v30
	v_mul_f32_e32 v181, 0xc01d265f, v31
	v_mul_f32_e32 v182, 0xc01d265f, v32
	v_mul_f32_e32 v183, 0xc01d265f, v33
	v_exp_f32_e32 v180, v180
	v_exp_f32_e32 v181, v181
	v_exp_f32_e32 v182, v182
	v_exp_f32_e32 v183, v183
	v_fmamk_f32 v26, v26, 0x3d000000, v91
	v_fmamk_f32 v27, v27, 0x3d000000, v93
	v_fmamk_f32 v28, v28, 0x3d000000, v83
	v_fmamk_f32 v29, v29, 0x3d000000, v85
	v_add_f32_e32 v180, 1.0, v180
	v_add_f32_e32 v181, 1.0, v181
	v_add_f32_e32 v182, 1.0, v182
	v_add_f32_e32 v183, 1.0, v183
	v_rcp_f32_e32 v180, v180
	v_rcp_f32_e32 v181, v181
	v_rcp_f32_e32 v182, v182
	v_rcp_f32_e32 v183, v183
	v_med3_f32 v26, v26, s72, v178
	v_med3_f32 v27, v27, s72, v178
	v_med3_f32 v28, v28, s72, v178
	v_med3_f32 v29, v29, s72, v178
	v_mul_f32_e32 v180, v30, v180
	v_mul_f32_e32 v181, v31, v181
	v_mul_f32_e32 v182, v32, v182
	v_mul_f32_e32 v183, v33, v183
	v_mul_f32_e32 v180, v26, v180
	v_mul_f32_e32 v181, v27, v181
	v_mul_f32_e32 v182, v28, v182
	v_mul_f32_e32 v183, v29, v183
	v_cvt_pk_fp8_f32 v200, v180, v181
	v_cvt_pk_fp8_f32 v200, v182, v183 op_sel:[0,0,1]
	v_fmamk_f32 v22, v22, 0x3d000000, v74
	v_fmamk_f32 v23, v23, 0x3d000000, v76
	v_fmamk_f32 v24, v24, 0x3d000000, v66
	v_fmamk_f32 v25, v25, 0x3d000000, v68
	v_min_f32_e32 v22, 0x40e00000, v22
	v_min_f32_e32 v23, 0x40e00000, v23
	v_min_f32_e32 v24, 0x40e00000, v24
	v_min_f32_e32 v25, 0x40e00000, v25
	v_mul_f32_e32 v184, 0xc01d265f, v22
	v_mul_f32_e32 v185, 0xc01d265f, v23
	v_mul_f32_e32 v186, 0xc01d265f, v24
	v_mul_f32_e32 v187, 0xc01d265f, v25
	v_exp_f32_e32 v184, v184
	v_exp_f32_e32 v185, v185
	v_exp_f32_e32 v186, v186
	v_exp_f32_e32 v187, v187
	v_fmamk_f32 v18, v18, 0x3d000000, v75
	v_fmamk_f32 v19, v19, 0x3d000000, v77
	v_fmamk_f32 v20, v20, 0x3d000000, v67
	v_fmamk_f32 v21, v21, 0x3d000000, v69
	v_add_f32_e32 v184, 1.0, v184
	v_add_f32_e32 v185, 1.0, v185
	v_add_f32_e32 v186, 1.0, v186
	v_add_f32_e32 v187, 1.0, v187
	v_rcp_f32_e32 v184, v184
	v_rcp_f32_e32 v185, v185
	v_rcp_f32_e32 v186, v186
	v_rcp_f32_e32 v187, v187
	v_med3_f32 v18, v18, s72, v178
	v_med3_f32 v19, v19, s72, v178
	v_med3_f32 v20, v20, s72, v178
	v_med3_f32 v21, v21, s72, v178
	v_mul_f32_e32 v184, v22, v184
	v_mul_f32_e32 v185, v23, v185
	v_mul_f32_e32 v186, v24, v186
	v_mul_f32_e32 v187, v25, v187
	v_mul_f32_e32 v184, v18, v184
	v_mul_f32_e32 v185, v19, v185
	v_mul_f32_e32 v186, v20, v186
	v_mul_f32_e32 v187, v21, v187
	v_cvt_pk_fp8_f32 v201, v184, v185
	v_cvt_pk_fp8_f32 v201, v186, v187 op_sel:[0,0,1]
	ds_bpermute_b32 v200, v199, v200
	ds_bpermute_b32 v201, v199, v201
	s_waitcnt lgkmcnt(2)
	global_store_dwordx2 v[210:211], v[204:205], off
	s_mov_b32 s98, 0x2c000
	v_lshl_add_u64 v[214:215], v[176:177], 0, s[98:99]
	v_fmamk_f32 v14, v14, 0x3d000000, v90
	v_fmamk_f32 v15, v15, 0x3d000000, v92
	v_fmamk_f32 v16, v16, 0x3d000000, v82
	v_fmamk_f32 v17, v17, 0x3d000000, v84
	v_min_f32_e32 v14, 0x40e00000, v14
	v_min_f32_e32 v15, 0x40e00000, v15
	v_min_f32_e32 v16, 0x40e00000, v16
	v_min_f32_e32 v17, 0x40e00000, v17
	v_mul_f32_e32 v180, 0xc01d265f, v14
	v_mul_f32_e32 v181, 0xc01d265f, v15
	v_mul_f32_e32 v182, 0xc01d265f, v16
	v_mul_f32_e32 v183, 0xc01d265f, v17
	v_exp_f32_e32 v180, v180
	v_exp_f32_e32 v181, v181
	v_exp_f32_e32 v182, v182
	v_exp_f32_e32 v183, v183
	v_fmamk_f32 v10, v10, 0x3d000000, v91
	v_fmamk_f32 v11, v11, 0x3d000000, v93
	v_fmamk_f32 v12, v12, 0x3d000000, v83
	v_fmamk_f32 v13, v13, 0x3d000000, v85
	v_add_f32_e32 v180, 1.0, v180
	v_add_f32_e32 v181, 1.0, v181
	v_add_f32_e32 v182, 1.0, v182
	v_add_f32_e32 v183, 1.0, v183
	v_rcp_f32_e32 v180, v180
	v_rcp_f32_e32 v181, v181
	v_rcp_f32_e32 v182, v182
	v_rcp_f32_e32 v183, v183
	v_med3_f32 v10, v10, s72, v178
	v_med3_f32 v11, v11, s72, v178
	v_med3_f32 v12, v12, s72, v178
	v_med3_f32 v13, v13, s72, v178
	v_mul_f32_e32 v180, v14, v180
	v_mul_f32_e32 v181, v15, v181
	v_mul_f32_e32 v182, v16, v182
	v_mul_f32_e32 v183, v17, v183
	v_mul_f32_e32 v180, v10, v180
	v_mul_f32_e32 v181, v11, v181
	v_mul_f32_e32 v182, v12, v182
	v_mul_f32_e32 v183, v13, v183
	v_cvt_pk_fp8_f32 v202, v180, v181
	v_cvt_pk_fp8_f32 v202, v182, v183 op_sel:[0,0,1]
	v_fmamk_f32 v6, v6, 0x3d000000, v74
	v_fmamk_f32 v7, v7, 0x3d000000, v76
	v_fmamk_f32 v8, v8, 0x3d000000, v66
	v_fmamk_f32 v9, v9, 0x3d000000, v68
	v_min_f32_e32 v6, 0x40e00000, v6
	v_min_f32_e32 v7, 0x40e00000, v7
	v_min_f32_e32 v8, 0x40e00000, v8
	v_min_f32_e32 v9, 0x40e00000, v9
	v_mul_f32_e32 v184, 0xc01d265f, v6
	v_mul_f32_e32 v185, 0xc01d265f, v7
	v_mul_f32_e32 v186, 0xc01d265f, v8
	v_mul_f32_e32 v187, 0xc01d265f, v9
	v_exp_f32_e32 v184, v184
	v_exp_f32_e32 v185, v185
	v_exp_f32_e32 v186, v186
	v_exp_f32_e32 v187, v187
	v_fmamk_f32 v2, v2, 0x3d000000, v75
	v_fmamk_f32 v3, v3, 0x3d000000, v77
	v_fmamk_f32 v4, v4, 0x3d000000, v67
	v_fmamk_f32 v5, v5, 0x3d000000, v69
	v_add_f32_e32 v184, 1.0, v184
	v_add_f32_e32 v185, 1.0, v185
	v_add_f32_e32 v186, 1.0, v186
	v_add_f32_e32 v187, 1.0, v187
	v_rcp_f32_e32 v184, v184
	v_rcp_f32_e32 v185, v185
	v_rcp_f32_e32 v186, v186
	v_rcp_f32_e32 v187, v187
	v_med3_f32 v2, v2, s72, v178
	v_med3_f32 v3, v3, s72, v178
	v_med3_f32 v4, v4, s72, v178
	v_med3_f32 v5, v5, s72, v178
	v_mul_f32_e32 v184, v6, v184
	v_mul_f32_e32 v185, v7, v185
	v_mul_f32_e32 v186, v8, v186
	v_mul_f32_e32 v187, v9, v187
	v_mul_f32_e32 v184, v2, v184
	v_mul_f32_e32 v185, v3, v185
	v_mul_f32_e32 v186, v4, v186
	v_mul_f32_e32 v187, v5, v187
	v_cvt_pk_fp8_f32 v203, v184, v185
	v_cvt_pk_fp8_f32 v203, v186, v187 op_sel:[0,0,1]
	ds_bpermute_b32 v202, v199, v202
	ds_bpermute_b32 v203, v199, v203
	s_waitcnt lgkmcnt(2)
	global_store_dwordx2 v[212:213], v[200:201], off
	s_waitcnt lgkmcnt(0)
	global_store_dwordx2 v[214:215], v[202:203], off
	s_cbranch_vccnz .LBB0_1239
	s_andn2_b64 vcc, exec, s[10:11]
	s_cbranch_vccnz .LBB0_1238
	s_barrier
	s_branch .LBB0_1238
